# speedup vs baseline: 1.0002x; 1.0002x over previous
_Z10gru_kernelPKhPf:
	s_load_dwordx4 s[8:11], s[0:1], 0x0
	s_lshr_b32 s20, s2, 1
	s_and_b32 s20, s20, 0x7fffffc
	s_and_b32 s21, s2, 3
	s_or_b32 s20, s20, s21
	s_lshl_b32 s20, s20, 12
	s_add_u32 s20, s20, 0x49000
	v_lshlrev_b32_e32 v249, 3, v0
	s_waitcnt lgkmcnt(0)
	s_add_u32 s20, s8, s20
	s_addc_u32 s21, s9, 0
	global_load_dwordx2 v[250:251], v249, s[20:21]
	s_bfe_u32 s16, s2, 0x10002
	v_mov_b32_e32 v157, 0
	v_lshrrev_b32_e32 v108, 6, v0
	v_and_b32_e32 v4, 63, v0
	s_movk_i32 s0, 0x1000
	v_mov_b32_e32 v9, v157
	v_lshl_or_b32 v1, s16, 3, v108
	v_mul_u32_u24_e32 v1, 0x300, v1
	v_lshlrev_b32_e32 v156, 4, v1
	v_lshl_add_u64 v[2:3], s[8:9], 0, v[156:157]
	v_lshlrev_b32_e32 v156, 4, v4
	v_lshl_add_u64 v[2:3], v[2:3], 0, v[156:157]
	v_add_co_u32_e64 v4, s[0:1], s0, v2
	v_lshl_or_b32 v1, s16, 4, v108
	s_nop 0
	v_addc_co_u32_e64 v5, s[0:1], 0, v3, s[0:1]
	s_movk_i32 s0, 0x2000
	s_nop 0
	v_add_co_u32_e64 v6, s[0:1], s0, v2
	v_or_b32_e32 v8, 8, v1
	s_nop 0
	v_addc_co_u32_e64 v7, s[0:1], 0, v3, s[0:1]
	s_add_u32 s0, s8, 0x30000
	v_mul_u32_u24_e32 v8, 0xc0, v8
	s_addc_u32 s1, s9, 0
	v_lshlrev_b32_e32 v8, 4, v8
	v_mul_u32_u24_e32 v1, 0xc0, v1
	v_lshl_add_u64 v[92:93], s[0:1], 0, v[8:9]
	v_lshlrev_b32_e32 v8, 4, v1
	v_lshl_add_u64 v[8:9], s[0:1], 0, v[8:9]
	s_lshl_b32 s0, s16, 11
	s_add_u32 s0, s8, s0
	s_addc_u32 s1, s9, 0
	v_and_b32_e32 v10, 0x1c0, v0
	v_mov_b32_e32 v11, v157
	v_lshl_add_u64 v[10:11], s[0:1], 0, v[10:11]
	v_and_b32_e32 v12, 48, v0
	v_mov_b32_e32 v13, v157
	v_and_b32_e32 v161, 15, v0
	v_lshl_add_u64 v[10:11], v[10:11], 0, v[12:13]
	s_mov_b64 s[0:1], 0x48000
	v_lshrrev_b32_e32 v12, 5, v0
	v_bfe_u32 v13, v0, 5, 1
	v_bfe_u32 v109, v0, 4, 2
	v_lshl_add_u64 v[72:73], v[10:11], 0, s[0:1]
	s_mov_b32 s0, 0x48000
	v_lshlrev_b32_e32 v1, 3, v0
	v_and_or_b32 v12, v12, 2, v13
	v_lshlrev_b32_e32 v13, 4, v161
	v_lshrrev_b32_e32 v14, 1, v0
	v_add_co_u32_e64 v10, s[0:1], s0, v10
	v_and_b32_e32 v1, 0xc00, v1
	v_lshl_or_b32 v12, v12, 8, v13
	v_and_b32_e32 v14, 8, v14
	v_lshl_add_u64 v[8:9], v[8:9], 0, v[156:157]
	v_addc_co_u32_e64 v11, s[0:1], 0, v11, s[0:1]
	v_or3_b32 v163, v12, v1, v14
	global_load_dwordx4 v[12:15], v[2:3], off
	global_load_dwordx4 v[16:19], v[2:3], off offset:1024
	global_load_dwordx4 v[20:23], v[2:3], off offset:2048
	global_load_dwordx4 v[24:27], v[2:3], off offset:3072
	global_load_dwordx4 v[28:31], v[6:7], off offset:-4096
	global_load_dwordx4 v[32:35], v[6:7], off
	global_load_dwordx4 v[36:39], v[6:7], off offset:1024
	global_load_dwordx4 v[40:43], v[6:7], off offset:2048
	global_load_dwordx4 v[44:47], v[6:7], off offset:3072
	global_load_dwordx4 v[48:51], v[4:5], off offset:1024
	global_load_dwordx4 v[52:55], v[4:5], off offset:2048
	global_load_dwordx4 v[56:59], v[4:5], off offset:3072
	global_load_dwordx4 v[60:63], v[8:9], off
	global_load_dwordx4 v[64:67], v[8:9], off offset:1024
	global_load_dwordx4 v[68:71], v[8:9], off offset:2048
	global_load_dwordx4 v[76:79], v[72:73], off offset:512
	global_load_dwordx4 v[80:83], v[72:73], off offset:1024
	global_load_dwordx4 v[84:87], v[10:11], off
	global_load_dwordx4 v[88:91], v[72:73], off offset:1536
	v_lshl_add_u64 v[164:165], v[92:93], 0, v[156:157]
	global_load_dwordx4 v[206:209], v[164:165], off
	global_load_dwordx4 v[210:213], v[164:165], off offset:1024
	global_load_dwordx4 v[214:217], v[164:165], off offset:2048
	s_movk_i32 s0, 0x200
	v_cmp_gt_u32_e32 vcc, s0, v0
	s_and_saveexec_b64 s[0:1], vcc
	s_cbranch_execz .LBB1_2
	v_mov_b32_e32 v2, 0
	v_lshlrev_b32_e32 v1, 4, v0
	v_mov_b32_e32 v3, v2
	v_mov_b32_e32 v4, v2
	v_mov_b32_e32 v5, v2
	ds_write_b128 v1, v[2:5]

.LBB1_4:
	v_mul_u32_u24_e32 v11, 0xfc1, v4
	s_mov_b32 s15, s14
	v_lshrrev_b32_e32 v218, 21, v11
	v_mul_u32_u24_e32 v11, 0xfc1, v5
	s_or_b64 s[0:1], s[14:15], s[6:7]
	v_lshrrev_b32_e32 v219, 3, v4
	v_lshrrev_b32_e32 v1, 3, v5
	v_lshrrev_b32_e32 v11, 21, v11
	v_cmp_le_u32_e32 vcc, s1, v3
	v_cmp_le_u32_e64 s[0:1], s0, v2
	v_mad_i32_i24 v1, v11, s3, v1
	v_mad_i32_i24 v219, v218, s3, v219
	s_and_saveexec_b64 s[16:17], s[0:1]
	s_cbranch_execz .LBB1_6
	v_lshl_or_b32 v218, v218, 3, v7
	v_cmp_eq_u32_e64 s[0:1], v218, v219
	v_cmp_gt_i32_e64 s[4:5], 64, v219
	s_and_b64 s[0:1], s[4:5], s[0:1]
	v_cndmask_b32_e64 v218, 0, v10, s[0:1]
	ds_write_b16 v9, v218

.LBB1_8:
	s_or_b64 exec, exec, s[12:13]
	s_mov_b32 s14, 0
	v_cmp_eq_u32_e32 vcc, 0, v0
	s_and_saveexec_b64 s[0:1], vcc
	v_mov_b32_e32 v1, 0
	ds_write_b32 v1, v1 offset:24832
	s_or_b64 exec, exec, s[0:1]
	s_lshr_b32 s0, s2, 1
	s_and_b32 s0, s0, 0x7fffffc
	s_and_b32 s1, s2, 3
	s_or_b32 s0, s0, s1
	s_bfe_u32 s16, s2, 0x10002
	s_lshl_b32 s2, s0, 5
	s_ashr_i32 s3, s2, 31
	s_lshl_b64 s[0:1], s[2:3], 7
	s_waitcnt lgkmcnt(0)
	s_add_u32 s0, s8, s0
	s_addc_u32 s1, s9, s1
	s_add_u32 s4, s0, 0x49000
	s_addc_u32 s5, s1, 0
	v_add_u32_e32 v5, 1, v2
	s_cmp_eq_u32 s16, 0
	v_lshlrev_b32_e32 v1, 9, v5
	s_cselect_b64 vcc, -1, 0
	v_add_u32_e32 v2, 0x4080, v6
	v_sub_u32_e32 v4, 0, v0
	v_and_b32_e32 v3, 0x3800, v1
	s_mov_b64 s[6:7], 0
	v_mov_b32_e32 v1, 0
	s_movk_i32 s15, 0xff7e
	s_movk_i32 s17, 0x80
	s_mov_b32 s18, 0
	s_barrier
	v_lshrrev_b32_e32 v4, 4, v0
	v_and_b32_e32 v5, 15, v0
	v_mul_u32_u24_e32 v4, 0x104, v4
	v_lshlrev_b32_e32 v5, 4, v5
	v_mov_b32_e32 v6, 0x4000400
	ds_write_b32 v4, v6 offset:16768
	s_waitcnt vmcnt(22)
	s_mov_b32 s0, 0xe0e0e0e0
	s_mov_b32 s1, 0x20202020
	s_mov_b32 s6, 0x01010101
	s_mov_b32 s7, 0x80808080
	v_and_b32_e32 v7, s0, v250
	v_xor_b32_e32 v7, s1, v7
	v_subrev_u32_e32 v9, s6, v7
	v_not_b32_e32 v7, v7
	v_and_b32_e32 v7, v9, v7
	v_and_b32_e32 v7, s7, v7
	v_and_b32_e32 v8, s0, v251
	v_xor_b32_e32 v8, s1, v8
	v_subrev_u32_e32 v9, s6, v8
	v_not_b32_e32 v8, v8
	v_and_b32_e32 v8, v9, v8
	v_and_b32_e32 v8, s7, v8
	v_or_b32_e32 v7, v7, v8
	v_bfe_u32 v8, v250, 0, 8
	v_bfe_u32 v9, v250, 8, 8
	v_min_u32_e32 v8, 64, v8
	v_min_u32_e32 v9, 64, v9
	v_lshlrev_b32_e32 v8, 4, v8
	v_lshlrev_b32_e32 v9, 20, v9
	v_or_b32_e32 v10, v8, v9
	v_bfe_u32 v8, v250, 16, 8
	v_bfe_u32 v9, v250, 24, 8
	v_min_u32_e32 v8, 64, v8
	v_min_u32_e32 v9, 64, v9
	v_lshlrev_b32_e32 v8, 4, v8
	v_lshlrev_b32_e32 v9, 20, v9
	v_or_b32_e32 v11, v8, v9
	v_bfe_u32 v8, v251, 0, 8
	v_bfe_u32 v9, v251, 8, 8
	v_min_u32_e32 v8, 64, v8
	v_min_u32_e32 v9, 64, v9
	v_lshlrev_b32_e32 v8, 4, v8
	v_lshlrev_b32_e32 v9, 20, v9
	v_or_b32_e32 v218, v8, v9
	v_bfe_u32 v8, v251, 16, 8
	v_bfe_u32 v9, v251, 24, 8
	v_min_u32_e32 v8, 64, v8
	v_min_u32_e32 v9, 64, v9
	v_lshlrev_b32_e32 v8, 4, v8
	v_lshlrev_b32_e32 v9, 20, v9
	v_or_b32_e32 v219, v8, v9
	s_cmp_eq_u32 s16, 0
	s_cbranch_scc0 .Ltok_bwd
	v_add_u32_e32 v4, v4, v5
	ds_write_b32 v4, v10 offset:16512
	ds_write_b32 v4, v11 offset:16516
	ds_write_b32 v4, v218 offset:16520
	ds_write_b32 v4, v219 offset:16524
	s_branch .Ltok_done
.Ltok_bwd:
	v_sub_u32_e32 v4, v4, v5
	v_alignbit_b32 v10, v10, v10, 16
	v_alignbit_b32 v11, v11, v11, 16
	v_alignbit_b32 v218, v218, v218, 16
	v_alignbit_b32 v219, v219, v219, 16
	ds_write_b32 v4, v219 offset:16752
	ds_write_b32 v4, v218 offset:16756
	ds_write_b32 v4, v11 offset:16760
	ds_write_b32 v4, v10 offset:16764
.Ltok_done:
	v_cmp_ne_u32_e32 vcc, 0, v7
	s_and_saveexec_b64 s[6:7], vcc
	v_mov_b32_e32 v1, 1
	v_mov_b32_e32 v2, 0
	ds_write_b32 v2, v1 offset:24832
	s_or_b64 exec, exec, s[6:7]
	s_mov_b32 s5, 0
	s_cmp_eq_u32 s16, 0
	s_cselect_b64 vcc, -1, 0
	v_mov_b32_e32 v157, 0
	s_waitcnt lgkmcnt(0)
	s_barrier
	s_and_b64 s[0:1], vcc, exec
	s_cselect_b32 s14, 0, 0x7f
	s_lshl_b32 s7, s16, 22
	s_add_u32 s0, s8, s7
	s_addc_u32 s1, s9, 0
	v_lshlrev_b32_e32 v94, 12, v108
	v_mov_b32_e32 v95, v157
	v_lshl_add_u64 v[0:1], s[0:1], 0, v[94:95]
	v_lshl_add_u64 v[0:1], v[0:1], 0, v[156:157]
	s_mov_b64 s[0:1], 0xc9000
	v_lshl_add_u64 v[158:159], v[0:1], 0, s[0:1]
	s_lshl_b32 s4, s14, 15
	v_lshl_add_u64 v[96:97], v[158:159], 0, s[4:5]
	global_load_dwordx4 v[72:75], v[96:97], off
	global_load_dwordx4 v[8:11], v[96:97], off offset:1024
	global_load_dwordx4 v[4:7], v[96:97], off offset:2048
	global_load_dwordx4 v[0:3], v[96:97], off offset:3072
	v_mul_u32_u24_e32 v95, 0x104, v161
	ds_read_b32 v96, v95 offset:16512
	ds_read_b32 v95, v95 offset:20672
	s_movk_i32 s6, 0x410
	s_movk_i32 s0, 0x104
	v_mov_b32_e32 v97, 0x4080
	s_waitcnt lgkmcnt(1)
	v_lshrrev_b32_e32 v178, 16, v96
	v_and_b32_e32 v96, 0xffff, v96
	v_mad_u32_u24 v176, v161, s0, v97
	v_mad_u32_u24 v110, v109, s6, v96
	s_waitcnt lgkmcnt(0)
	v_lshrrev_b32_e32 v177, 16, v95
	v_and_b32_e32 v95, 0xffff, v95
	s_and_b64 s[0:1], vcc, exec
	v_mad_u32_u24 v111, v109, s6, v95
	s_cselect_b32 s15, 1, -1
	s_or_b32 s0, s7, s4
	ds_read_b128 v[120:123], v110 offset:8192
	ds_read_b128 v[116:119], v111 offset:8192
	v_or3_b32 v92, s0, v94, v156
	v_mov_b32_e32 v93, v157
	v_lshl_add_u64 v[92:93], s[8:9], 0, v[92:93]
	s_mov_b64 s[0:1], 0xc9800
	s_lshl_b32 s4, s15, 1
	v_mov_b32_e32 v106, v157
	v_mov_b32_e32 v107, v157
	v_lshl_add_u64 v[166:167], v[92:93], 0, s[0:1]
	s_ashr_i32 s5, s4, 31
	v_mov_b32_e32 v100, 0xc47a0000
	v_mov_b32_e32 v104, v157
	v_mov_b32_e32 v105, v157
	v_mov_b32_e32 v92, 0
	v_mov_b64_e32 v[142:143], v[106:107]
	s_lshl_b64 s[6:7], s[4:5], 15
	s_add_i32 s8, s14, s15
	v_mov_b32_e32 v101, v100
	v_mov_b32_e32 v102, v100
	v_mov_b32_e32 v103, v100
	s_mov_b32 s5, -2
	v_cmp_ne_u32_e64 s[0:1], 1, v92
	v_mov_b32_e32 v172, v157
	v_mov_b32_e32 v173, v157
	v_mov_b32_e32 v174, v157
	v_mov_b32_e32 v175, v157
	v_mov_b32_e32 v96, v157
	v_mov_b32_e32 v97, v157
	v_mov_b32_e32 v98, v157
	v_mov_b32_e32 v99, v157
	v_mov_b32_e32 v92, v157
	v_mov_b32_e32 v93, v157
	v_mov_b32_e32 v94, v157
	v_mov_b32_e32 v95, v157
	v_mov_b32_e32 v144, v157
	v_mov_b32_e32 v145, v157
	v_mov_b32_e32 v146, v157
	v_mov_b32_e32 v147, v157
	v_mov_b32_e32 v132, v157
	v_mov_b32_e32 v133, v157
	v_mov_b32_e32 v134, v157
	v_mov_b32_e32 v135, v157
	v_mov_b32_e32 v128, v157
	v_mov_b32_e32 v129, v157
	v_mov_b32_e32 v130, v157
	v_mov_b32_e32 v131, v157
	v_mov_b32_e32 v136, v157
	v_mov_b32_e32 v137, v157
	v_mov_b32_e32 v138, v157
	v_mov_b32_e32 v139, v157
	v_mov_b32_e32 v124, v157
	v_mov_b32_e32 v125, v157
	v_mov_b32_e32 v126, v157
	v_mov_b32_e32 v127, v157
	v_mov_b32_e32 v170, v157
	v_mov_b32_e32 v171, v157
	v_mov_b32_e32 v168, v157
	v_mov_b32_e32 v169, v157
	v_lshlrev_b32_e32 v162, 4, v108
	v_mul_u32_u24_e32 v157, 0x410, v109
	v_lshlrev_b32_e32 v160, 2, v109
	v_mov_b64_e32 v[140:141], v[104:105]
	v_mov_b32_e32 v144, 0
	v_mov_b32_e32 v145, 0
	v_mov_b32_e32 v146, 0
	v_mov_b32_e32 v147, 0
	v_mov_b32_e32 v148, 0xc47a0000
	v_mov_b32_e32 v149, 0xc47a0000
	v_mov_b32_e32 v150, 0xc47a0000
	v_mov_b32_e32 v151, 0xc47a0000
	v_mov_b32_e32 v152, 0
	v_mov_b32_e32 v153, 0
	v_mov_b32_e32 v154, 0
	v_mov_b32_e32 v155, 0
	s_movk_i32 s17, 0x61
	v_add_u32_e32 v226, v162, v160
	v_mul_u32_u24_e32 v226, 12, v226
	v_lshl_add_u32 v229, v161, 4, v157
	v_mul_u32_u24_e32 v230, 0x610, v161
	v_add_u32_e32 v230, v230, v226
	v_add_u32_e32 v231, 0x18400, v226
	s_waitcnt vmcnt(4) lgkmcnt(0)
	ds_read_b128 v[190:193], v229 offset:8192
	s_waitcnt lgkmcnt(0)
	v_mfma_f32_16x16x32_f16 v[194:197], v[60:63], v[190:193], v[84:87]
	v_mfma_f32_16x16x32_f16 v[198:201], v[64:67], v[190:193], v[76:79]
	v_mfma_f32_16x16x32_f16 v[202:205], v[68:71], v[190:193], v[88:91]
	s_nop 7
	s_nop 1
	ds_write_b128 v230, v[194:197] offset:24848
	ds_write_b128 v230, v[198:201] offset:24864
	ds_write_b128 v230, v[202:205] offset:24880
	v_add_u32_e32 v230, 0x6100, v230
	ds_read_b128 v[190:193], v229 offset:8448
	s_waitcnt lgkmcnt(0)
	v_mfma_f32_16x16x32_f16 v[194:197], v[60:63], v[190:193], v[84:87]
	v_mfma_f32_16x16x32_f16 v[198:201], v[64:67], v[190:193], v[76:79]
	v_mfma_f32_16x16x32_f16 v[202:205], v[68:71], v[190:193], v[88:91]
	s_nop 7
	s_nop 1
	ds_write_b128 v230, v[194:197] offset:24848
	ds_write_b128 v230, v[198:201] offset:24864
	ds_write_b128 v230, v[202:205] offset:24880
	v_add_u32_e32 v230, 0x6100, v230
	ds_read_b128 v[190:193], v229 offset:12864
	s_waitcnt lgkmcnt(0)
	v_mfma_f32_16x16x32_f16 v[194:197], v[206:209], v[190:193], v[84:87]
	v_mfma_f32_16x16x32_f16 v[198:201], v[210:213], v[190:193], v[76:79]
	v_mfma_f32_16x16x32_f16 v[202:205], v[214:217], v[190:193], v[88:91]
	s_nop 7
	s_nop 1
	ds_write_b128 v230, v[194:197] offset:24848
	ds_write_b128 v230, v[198:201] offset:24864
	ds_write_b128 v230, v[202:205] offset:24880
	v_add_u32_e32 v230, 0x6100, v230
	ds_read_b128 v[190:193], v229 offset:13120
	s_waitcnt lgkmcnt(0)
	v_mfma_f32_16x16x32_f16 v[194:197], v[206:209], v[190:193], v[84:87]
	v_mfma_f32_16x16x32_f16 v[198:201], v[210:213], v[190:193], v[76:79]
	v_mfma_f32_16x16x32_f16 v[202:205], v[214:217], v[190:193], v[88:91]
	s_nop 7
	s_nop 1
	ds_write_b128 v230, v[194:197] offset:24848
	ds_write_b128 v230, v[198:201] offset:24864
	ds_write_b128 v230, v[202:205] offset:24880
	ds_write_b128 v231, v[84:87] offset:24848
	ds_write_b128 v231, v[76:79] offset:24864
	ds_write_b128 v231, v[88:91] offset:24880
	ds_read_u16 v232, v176
	ds_read_u16 v177, v176 offset:4160
	s_waitcnt lgkmcnt(0)
	v_mad_u32_u24 v227, v232, s17, v226
	ds_read_b128 v[116:119], v227 offset:24848
	ds_read_b128 v[120:123], v227 offset:24864
	ds_read_b128 v[138:141], v227 offset:24880
	v_mov_b32_e32 v182, 0
	v_mov_b32_e32 v183, 0
	v_mov_b32_e32 v184, 0
	v_mov_b32_e32 v185, 0
	v_mov_b32_e32 v222, 0
	v_mov_b32_e32 v223, 0
	v_mov_b32_e32 v224, 0
	v_mov_b32_e32 v225, 0
	v_mov_b32_e32 v186, 0
	v_mov_b32_e32 v187, 0
	v_mov_b32_e32 v188, 0
	v_mov_b32_e32 v189, 0
	v_mov_b32_e32 v100, 0
	v_mov_b32_e32 v101, 0
	v_mov_b32_e32 v102, 0
	v_mov_b32_e32 v103, 0
	v_mov_b32_e32 v104, 0
	v_mov_b32_e32 v105, 0
	v_mov_b32_e32 v106, 0
	v_mov_b32_e32 v107, 0
	v_mov_b32_e32 v108, 0
	v_mov_b32_e32 v109, 0
	v_mov_b32_e32 v110, 0
	v_mov_b32_e32 v111, 0
	v_mov_b32_e32 v112, 0
	v_mov_b32_e32 v113, 0
	v_mov_b32_e32 v114, 0
	v_mov_b32_e32 v115, 0
	v_mov_b32_e32 v206, 0
	v_mov_b32_e32 v207, 0
	v_mov_b32_e32 v208, 0
	v_mov_b32_e32 v209, 0
	v_mov_b32_e32 v210, 0
	v_mov_b32_e32 v211, 0
	v_mov_b32_e32 v212, 0
	v_mov_b32_e32 v213, 0
	v_mov_b32_e32 v214, 0
	v_mov_b32_e32 v215, 0
	v_mov_b32_e32 v216, 0
	v_mov_b32_e32 v217, 0
	v_mov_b32_e32 v218, 0
	v_mov_b32_e32 v219, 0
	v_mov_b32_e32 v220, 0
	v_mov_b32_e32 v221, 0
	s_waitcnt vmcnt(4) lgkmcnt(0)
	v_readfirstlane_b32 s18, v162
	s_nop 3
	s_cmp_ge_u32 s18, 64
	s_cbranch_scc1 .Lgru_loop_b
